# baseline (speedup 1.0000x reference)
_Z9fc_kernelPKDv8_DF16_S1_Pf:
	s_cmp_gt_u32 s2, 195
	s_cbranch_scc1 .Lfc_exit
	s_load_dwordx4 s[4:7], s[0:1], 0x0
	s_load_dwordx2 s[16:17], s[0:1], 0x10
	v_and_b32_e32 v1, 63, v0
	v_lshrrev_b32_e32 v113, 6, v0
	v_and_b32_e32 v89, 31, v0
	v_bfe_u32 v90, v0, 5, 1
	v_lshlrev_b32_e32 v116, 4, v0
	v_lshlrev_b32_e32 v112, 4, v1
	v_lshlrev_b32_e32 v4, 12, v90
	v_lshl_or_b32 v4, v113, 8, v4
	v_lshl_or_b32 v4, v89, 2, v4
	v_add_u32_e32 v102, 0x1c000, v4
	v_lshlrev_b32_e32 v5, 10, v113
	s_mov_b32 s3, 0x1c000
	v_add3_u32 v103, v5, v112, s3
	v_mul_u32_u24_e32 v6, 0x30d40, v113
	v_add_u32_e32 v104, v6, v112
	v_add_u32_e32 v105, 0x61a80, v104
	v_add_u32_e32 v106, 0xc3500, v104
	v_add_u32_e32 v107, 0x124f80, v104
	v_add_u32_e32 v108, 0x186a00, v104
	v_add_u32_e32 v109, 0x1e8480, v104
	v_add_u32_e32 v110, 0x249f00, v104
	v_add_u32_e32 v111, 0x2ab980, v104
	v_readfirstlane_b32 s38, v113
	v_mul_u32_u24_e32 v7, 0x3800, v113
	v_add_u32_e32 v114, v7, v112
	v_cmp_gt_u32_e64 s[34:35], 20, v1
	s_mul_i32 s3, s2, 0xe000
	v_add_u32_e32 v117, s3, v114
	v_add_u32_e32 v118, 0x1000, v117
	v_add_u32_e32 v119, 0x2000, v117
	v_add_u32_e32 v115, 0x3000, v117
	s_waitcnt lgkmcnt(0)
	global_load_dwordx4 v[32:35], v117, s[4:5]
	global_load_dwordx4 v[36:39], v117, s[4:5] offset:1024
	global_load_dwordx4 v[40:43], v117, s[4:5] offset:2048
	global_load_dwordx4 v[44:47], v117, s[4:5] offset:3072
	global_load_dwordx4 v[48:51], v118, s[4:5]
	global_load_dwordx4 v[52:55], v118, s[4:5] offset:1024
	global_load_dwordx4 v[56:59], v118, s[4:5] offset:2048
	global_load_dwordx4 v[60:63], v118, s[4:5] offset:3072
	global_load_dwordx4 v[64:67], v119, s[4:5]
	global_load_dwordx4 v[68:71], v119, s[4:5] offset:1024
	global_load_dwordx4 v[72:75], v119, s[4:5] offset:2048
	global_load_dwordx4 v[76:79], v119, s[4:5] offset:3072
	global_load_dwordx4 v[80:83], v115, s[4:5]
	global_load_dwordx4 v[84:87], v115, s[4:5] offset:1024
	s_mov_b64 s[30:31], s[6:7]
	global_load_dwordx4 v[152:155], v116, s[30:31]
	s_add_u32 s30, s30, 0x1000
	s_addc_u32 s31, s31, 0
	global_load_dwordx4 v[156:159], v116, s[30:31]
	s_add_u32 s30, s30, 0x1000
	s_addc_u32 s31, s31, 0
	global_load_dwordx4 v[160:163], v116, s[30:31]
	s_add_u32 s30, s30, 0x1000
	s_addc_u32 s31, s31, 0
	global_load_dwordx4 v[164:167], v116, s[30:31]
	s_add_u32 s30, s30, 0x1000
	s_addc_u32 s31, s31, 0
	global_load_dwordx4 v[168:171], v116, s[30:31]
	s_add_u32 s30, s30, 0x1000
	s_addc_u32 s31, s31, 0
	global_load_dwordx4 v[172:175], v116, s[30:31]
	s_add_u32 s30, s30, 0x1000
	s_addc_u32 s31, s31, 0
	global_load_dwordx4 v[176:179], v116, s[30:31]
	s_add_u32 s30, s30, 0x1000
	s_addc_u32 s31, s31, 0
	global_load_dwordx4 v[180:183], v116, s[30:31]
	s_add_u32 s30, s30, 0x1000
	s_addc_u32 s31, s31, 0
	global_load_dwordx4 v[184:187], v116, s[30:31]
	s_add_u32 s30, s30, 0x1000
	s_addc_u32 s31, s31, 0
	global_load_dwordx4 v[188:191], v116, s[30:31]
	s_add_u32 s30, s30, 0x1000
	s_addc_u32 s31, s31, 0
	global_load_dwordx4 v[192:195], v116, s[30:31]
	s_add_u32 s30, s30, 0x1000
	s_addc_u32 s31, s31, 0
	global_load_dwordx4 v[196:199], v116, s[30:31]
	s_add_u32 s30, s30, 0x1000
	s_addc_u32 s31, s31, 0
	global_load_dwordx4 v[200:203], v116, s[30:31]
	s_add_u32 s30, s30, 0x1000
	s_addc_u32 s31, s31, 0
	global_load_dwordx4 v[204:207], v116, s[30:31]
	s_lshl_b32 s3, s2, 10
	s_add_u32 s8, s16, s3
	s_addc_u32 s9, s17, 0
	s_add_u32 s12, s8, 0x30d400
	s_addc_u32 s13, s9, 0
	s_mov_b64 s[24:25], -1
	s_cmp_eq_u32 s2, 195
	s_cselect_b64 s[24:25], s[34:35], s[24:25]
	s_mov_b32 s20, 0
	s_waitcnt vmcnt(0)
	ds_write_b128 v116, v[152:155]
	ds_write_b128 v116, v[156:159] offset:4096
	ds_write_b128 v116, v[160:163] offset:8192
	ds_write_b128 v116, v[164:167] offset:12288
	ds_write_b128 v116, v[168:171] offset:16384
	ds_write_b128 v116, v[172:175] offset:20480
	ds_write_b128 v116, v[176:179] offset:24576
	ds_write_b128 v116, v[180:183] offset:28672
	ds_write_b128 v116, v[184:187] offset:32768
	ds_write_b128 v116, v[188:191] offset:36864
	ds_write_b128 v116, v[192:195] offset:40960
	ds_write_b128 v116, v[196:199] offset:45056
	ds_write_b128 v116, v[200:203] offset:49152
	ds_write_b128 v116, v[204:207] offset:53248
	s_waitcnt lgkmcnt(0)
	s_barrier

.Lfc_step:
	v_mfma_f32_32x32x16_f16 v[0:15], v[120:123], v[32:35], 0
	v_mfma_f32_32x32x16_f16 v[16:31], v[120:123], v[60:63], 0
	v_mfma_f32_32x32x16_f16 v[0:15], v[124:127], v[36:39], v[0:15]
	v_mfma_f32_32x32x16_f16 v[16:31], v[124:127], v[64:67], v[16:31]
	v_mfma_f32_32x32x16_f16 v[0:15], v[128:131], v[40:43], v[0:15]
	v_mfma_f32_32x32x16_f16 v[16:31], v[128:131], v[68:71], v[16:31]
	v_mfma_f32_32x32x16_f16 v[0:15], v[132:135], v[44:47], v[0:15]
	v_mfma_f32_32x32x16_f16 v[16:31], v[132:135], v[72:75], v[16:31]
	v_mfma_f32_32x32x16_f16 v[0:15], v[136:139], v[48:51], v[0:15]
	v_mfma_f32_32x32x16_f16 v[16:31], v[136:139], v[76:79], v[16:31]
	v_mfma_f32_32x32x16_f16 v[0:15], v[140:143], v[52:55], v[0:15]
	v_mfma_f32_32x32x16_f16 v[16:31], v[140:143], v[80:83], v[16:31]
	v_mfma_f32_32x32x16_f16 v[0:15], v[144:147], v[56:59], v[0:15]
	v_mfma_f32_32x32x16_f16 v[16:31], v[144:147], v[84:87], v[16:31]
	s_nop 11
	s_barrier
	ds_write_b32 v102, v0 offset:0
	ds_write_b32 v102, v1 offset:1024
	ds_write_b32 v102, v2 offset:2048
	ds_write_b32 v102, v3 offset:3072
	ds_write_b32 v102, v4 offset:8192
	ds_write_b32 v102, v5 offset:9216
	ds_write_b32 v102, v6 offset:10240
	ds_write_b32 v102, v7 offset:11264
	ds_write_b32 v102, v8 offset:16384
	ds_write_b32 v102, v9 offset:17408
	ds_write_b32 v102, v10 offset:18432
	ds_write_b32 v102, v11 offset:19456
	ds_write_b32 v102, v12 offset:24576
	ds_write_b32 v102, v13 offset:25600
	ds_write_b32 v102, v14 offset:26624
	ds_write_b32 v102, v15 offset:27648
	ds_write_b32 v102, v16 offset:128
	ds_write_b32 v102, v17 offset:1152
	ds_write_b32 v102, v18 offset:2176
	ds_write_b32 v102, v19 offset:3200
	ds_write_b32 v102, v20 offset:8320
	ds_write_b32 v102, v21 offset:9344
	ds_write_b32 v102, v22 offset:10368
	ds_write_b32 v102, v23 offset:11392
	ds_write_b32 v102, v24 offset:16512
	ds_write_b32 v102, v25 offset:17536
	ds_write_b32 v102, v26 offset:18560
	ds_write_b32 v102, v27 offset:19584
	ds_write_b32 v102, v28 offset:24704
	ds_write_b32 v102, v29 offset:25728
	ds_write_b32 v102, v30 offset:26752
	ds_write_b32 v102, v31 offset:27776
	s_waitcnt lgkmcnt(0)
	s_barrier
	ds_read_b128 v[120:123], v88
	ds_read_b128 v[124:127], v88 offset:1024
	ds_read_b128 v[128:131], v88 offset:2048
	ds_read_b128 v[132:135], v88 offset:3072
	ds_read_b128 v[136:139], v88 offset:4096
	ds_read_b128 v[140:143], v88 offset:5120
	ds_read_b128 v[144:147], v88 offset:6144
	v_add_u32_e32 v88, 0x1c00, v88
	s_cmp_ge_u32 s38, 2
	s_cbranch_scc1 .Lfc_nostore
	ds_read_b128 v[0:3], v103
	ds_read_b128 v[4:7], v103 offset:2048
	ds_read_b128 v[8:11], v103 offset:4096
	ds_read_b128 v[12:15], v103 offset:6144
	ds_read_b128 v[16:19], v103 offset:8192
	ds_read_b128 v[20:23], v103 offset:10240
	ds_read_b128 v[24:27], v103 offset:12288
	ds_read_b128 v[28:31], v103 offset:14336
	s_mov_b64 exec, s[24:25]
	s_waitcnt lgkmcnt(7)
	global_store_dwordx4 v104, v[0:3], s[8:9] nt
	s_waitcnt lgkmcnt(6)
	global_store_dwordx4 v105, v[4:7], s[8:9] nt
	s_waitcnt lgkmcnt(5)
	global_store_dwordx4 v106, v[8:11], s[8:9] nt
	s_waitcnt lgkmcnt(4)
	global_store_dwordx4 v107, v[12:15], s[8:9] nt
	s_waitcnt lgkmcnt(3)
	global_store_dwordx4 v108, v[16:19], s[8:9] nt
	s_waitcnt lgkmcnt(2)
	global_store_dwordx4 v109, v[20:23], s[8:9] nt
	s_waitcnt lgkmcnt(1)
	global_store_dwordx4 v110, v[24:27], s[8:9] nt
	s_waitcnt lgkmcnt(0)
	global_store_dwordx4 v111, v[28:31], s[8:9] nt
	s_mov_b64 exec, -1
	s_nop 1
	ds_read_b128 v[0:3], v103 offset:16384
	ds_read_b128 v[4:7], v103 offset:18432
	ds_read_b128 v[8:11], v103 offset:20480
	ds_read_b128 v[12:15], v103 offset:22528
	ds_read_b128 v[16:19], v103 offset:24576
	ds_read_b128 v[20:23], v103 offset:26624
	ds_read_b128 v[24:27], v103 offset:28672
	ds_read_b128 v[28:31], v103 offset:30720
	s_mov_b64 exec, s[24:25]
	s_waitcnt lgkmcnt(7)
	global_store_dwordx4 v104, v[0:3], s[12:13] nt
	s_waitcnt lgkmcnt(6)
	global_store_dwordx4 v105, v[4:7], s[12:13] nt
	s_waitcnt lgkmcnt(5)
	global_store_dwordx4 v106, v[8:11], s[12:13] nt
	s_waitcnt lgkmcnt(4)
	global_store_dwordx4 v107, v[12:15], s[12:13] nt
	s_waitcnt lgkmcnt(3)
	global_store_dwordx4 v108, v[16:19], s[12:13] nt
	s_waitcnt lgkmcnt(2)
	global_store_dwordx4 v109, v[20:23], s[12:13] nt
	s_waitcnt lgkmcnt(1)
	global_store_dwordx4 v110, v[24:27], s[12:13] nt
	s_waitcnt lgkmcnt(0)
	global_store_dwordx4 v111, v[28:31], s[12:13] nt
	s_mov_b64 exec, -1
	s_waitcnt vmcnt(16)
.Lfc_nostore:
	s_add_u32 s12, s12, 0x61a800
	s_addc_u32 s13, s13, 0
	s_add_u32 s8, s8, 0x61a800
	s_addc_u32 s9, s9, 0
	s_add_i32 s0, s0, 1
	s_cmp_lt_u32 s0, 8
	s_cbranch_scc1 .Lfc_step
	s_cmp_eq_u32 s20, 15
	s_cbranch_scc1 .Lfc_exit
	s_cmp_ge_u32 s38, 2
	s_cbranch_scc0 .Lfc_sw
	s_waitcnt vmcnt(0)
.Lfc_sw:
	s_waitcnt vmcnt(63)
	s_add_i32 s3, s20, 1
	s_and_b32 s3, s3, 1
	s_mul_i32 s3, s3, 0xe000
	v_add_u32_e32 v117, s3, v116
	ds_write_b128 v117, v[152:155]
	ds_write_b128 v117, v[156:159] offset:4096
	ds_write_b128 v117, v[160:163] offset:8192
	ds_write_b128 v117, v[164:167] offset:12288
	ds_write_b128 v117, v[168:171] offset:16384
	ds_write_b128 v117, v[172:175] offset:20480
	ds_write_b128 v117, v[176:179] offset:24576
	ds_write_b128 v117, v[180:183] offset:28672
	ds_write_b128 v117, v[184:187] offset:32768
	ds_write_b128 v117, v[188:191] offset:36864
	ds_write_b128 v117, v[192:195] offset:40960
	ds_write_b128 v117, v[196:199] offset:45056
	ds_write_b128 v117, v[200:203] offset:49152
	ds_write_b128 v117, v[204:207] offset:53248
	s_waitcnt lgkmcnt(0)
	s_barrier
	s_add_i32 s20, s20, 1
	s_branch .Lfc_seg
